# v20 + static s_setprio 1 for waves 4-7 during the attention phase
# speedup vs baseline: 1.0412x; 1.0000x over previous
; #define LAS __attribute__((address_space(3)))
; __device__ __forceinline__ int opaque_tid() { int t = threadIdx.x; asm volatile("" : "+v"(t)); return t; }
;     using namespace att;
;     const int tid = opaque_tid(), wid = __builtin_amdgcn_readfirstlane(tid >> 6);
;     const bf16_t* proj = (const bf16_t*)(a.ws + WS_PROJ);
;     bf16_t* mix = (bf16_t*)(a.ws + WS_ACT);
;     bf16_t* dilo = (bf16_t*)a.out;
;     float* dill = (float*)(a.ws + WS_DILL);
;     const float* cumall = (const float*)(a.ws + WS_CUM);
;     unsigned* queue = (unsigned*)(a.ws + WS_CTL) + CW_QUEUE + (layer + 2 * qslot) * 64;
;     LAS int* flags = (LAS int*)(lds + L_FLAG);
;     LAS int* info = (LAS int*)(lds + L_INFO);
;     LAS float* tab = (LAS float*)(lds + L_TAB);
;     LAS float* relb = (LAS float*)(lds + SEG_OFF + 256);
;     if (tid < 32 * 6) relb[tid] = a.in[I_RELB][tid] * LOG2E;
;     __syncthreads();
.LBB0_390:
	s_or_b64 exec, exec, s[38:39]
	v_readfirstlane_b32 vcc_lo, v0
	s_nop 1
	s_lshr_b32 vcc_lo, vcc_lo, 6
	s_cmp_ge_u32 vcc_lo, 4
	s_cbranch_scc0 .Lat_prio_skip
	s_setprio 1
.Lat_prio_skip:
	v_mov_b32_e32 v18, v0
	s_movk_i32 s2, 0xc0
	s_waitcnt lgkmcnt(0)
	s_barrier
	s_nop 0
	v_readfirstlane_b32 s12, v18
	v_cmp_gt_i32_e32 vcc, s2, v18
	s_and_saveexec_b64 s[4:5], vcc
	s_cbranch_execz .LBB0_392
	v_readlane_b32 s16, v252, 41
	v_ashrrev_i32_e32 v19, 31, v18
	v_readlane_b32 s17, v252, 42
	v_readlane_b32 s18, v252, 43
	v_readlane_b32 s19, v252, 44
	v_lshl_add_u64 v[2:3], v[18:19], 2, s[16:17]
	global_load_dword v1, v[2:3], off
	v_lshl_add_u32 v2, v18, 2, 0
	v_add_u32_e32 v2, 0x21f00, v2
	v_readlane_b32 s20, v252, 45
	v_readlane_b32 s21, v252, 46
	v_readlane_b32 s22, v252, 47
	v_readlane_b32 s23, v252, 48
	s_waitcnt vmcnt(0)
	v_mul_f32_e32 v1, 0x3fb8aa3b, v1
	ds_write_b32 v2, v1

; __device__ __forceinline__ int opaque_tid() { int t = threadIdx.x; asm volatile("" : "+v"(t)); return t; }
; __device__ __forceinline__ void mg_merge(const Args& a) {
;     const bf16_t* dilo = (const bf16_t*)a.out;
;     const float* dill = (const float*)(a.ws + WS_DILL);
;     bf16_t* mix = (bf16_t*)(a.ws + WS_ACT);
;     const int tid = opaque_tid();
;     const size_t total = (size_t)6 * NTOK * 8;
;     const size_t step = (size_t)gridDim.x * NTHR;
;     for (size_t i0 = (size_t)blockIdx.x * NTHR + tid; i0 < total; i0 += 4 * step) {
;         u32x4 a0[4], a1[4], a2[4]; float l0[4], l1[4], l2[4];
; #pragma unroll
;         for (int q = 0; q < 4; ++q) { const size_t i = i0 + q * step; if (i < total) { const size_t ht = i >> 3; const int c = (int)(i & 7);
.LBB0_645:
	s_or_b64 exec, exec, s[38:39]
	s_setprio 0
	v_mov_b32_e32 v2, v0
	v_readlane_b32 s4, v253, 15
	s_waitcnt lgkmcnt(0)
	s_barrier
	v_readlane_b32 s5, v253, 16
	v_ashrrev_i32_e32 v3, 31, v2
	s_nop 0
	v_lshl_add_u64 v[56:57], s[4:5], 0, v[2:3]
	s_mov_b64 s[4:5], 0x180000
	v_cmp_gt_u64_e32 vcc, s[4:5], v[56:57]
	s_and_saveexec_b64 s[10:11], vcc
	s_cbranch_execz .LBB0_660
	v_readlane_b32 s4, v254, 6
	v_readlane_b32 s5, v254, 7
	s_mov_b64 s[12:13], 0
	s_nop 0
	v_lshl_add_u64 v[52:53], v[2:3], 3, s[4:5]
	v_mov_b32_e32 v2, 0
	v_mov_b32_e32 v3, v2
	v_mov_b32_e32 v4, v2
	v_mov_b32_e32 v5, v2
	v_mov_b32_e32 v18, v2
	v_mov_b32_e32 v19, v2
	v_mov_b32_e32 v20, v2
	v_mov_b32_e32 v21, v2
	v_mov_b32_e32 v22, v2
	v_mov_b32_e32 v23, v2
	v_mov_b32_e32 v24, v2
	v_mov_b32_e32 v25, v2
	v_mov_b32_e32 v26, v2
	v_mov_b32_e32 v27, v2
	v_mov_b32_e32 v28, v2
	v_mov_b32_e32 v29, v2
	v_mov_b32_e32 v30, v2
	v_mov_b32_e32 v31, v2
	v_mov_b32_e32 v32, v2
	v_mov_b32_e32 v33, v2
	v_mov_b32_e32 v36, v2
	v_mov_b32_e32 v37, v2
	v_mov_b32_e32 v38, v2
	v_mov_b32_e32 v39, v2
	s_branch .LBB0_648
